# NSA tile loop: score copies eliminated (on top of the pipelined K/V fragment reads), placement kept
# speedup vs baseline: 1.0094x; 1.0094x over previous
.LBB0_2419:
	s_lshl_b32 s2, s2, 13
	s_add_i32 s76, s2, 0
	s_add_i32 s76, s76, 0x10000
	s_andn2_b64 vcc, exec, s[8:9]
	v_lshlrev_b32_e32 v134, 2, v162
	s_cbranch_vccnz .LBB0_2468
	v_or_b32_e32 v6, 32, v168
	v_cmp_gt_i32_e64 s[40:41], v6, v2
	v_cmp_lt_i32_e64 s[42:43], v6, v2
	v_or_b32_e32 v6, 34, v168
	v_cmp_gt_i32_e64 s[44:45], v6, v2
	v_or_b32_e32 v6, 35, v168
	v_cmp_gt_i32_e64 s[46:47], v6, v2
	v_or_b32_e32 v6, 40, v168
	v_cmp_gt_i32_e64 s[48:49], v6, v2
	v_or_b32_e32 v6, 41, v168
	v_cmp_gt_i32_e64 s[50:51], v6, v2
	v_or_b32_e32 v6, 42, v168
	v_cmp_gt_i32_e64 s[52:53], v6, v2
	v_or_b32_e32 v6, 43, v168
	v_cmp_gt_i32_e64 s[54:55], v6, v2
	v_or_b32_e32 v6, 48, v168
	v_cmp_gt_i32_e64 s[56:57], v6, v2
	v_or_b32_e32 v6, 49, v168
	v_cmp_gt_i32_e64 s[58:59], v6, v2
	v_or_b32_e32 v6, 50, v168
	v_cmp_gt_i32_e64 s[60:61], v6, v2
	v_or_b32_e32 v6, 51, v168
	v_cmp_gt_i32_e64 s[62:63], v6, v2
	v_or_b32_e32 v6, 56, v168
	v_cmp_gt_i32_e64 s[64:65], v6, v2
	v_or_b32_e32 v6, 57, v168
	v_cmp_gt_i32_e64 s[66:67], v6, v2
	v_or_b32_e32 v6, 58, v168
	v_cmp_gt_i32_e64 s[68:69], v6, v2
	v_or_b32_e32 v6, 59, v168
	v_cmp_gt_i32_e64 s[6:7], v168, v2
	v_cmp_lt_i32_e64 s[8:9], v168, v2
	v_cmp_gt_i32_e64 s[10:11], v135, v2
	v_cmp_gt_i32_e64 s[12:13], v169, v2
	v_cmp_gt_i32_e64 s[14:15], v170, v2
	v_cmp_gt_i32_e64 s[16:17], v171, v2
	v_cmp_gt_i32_e64 s[18:19], v172, v2
	v_cmp_gt_i32_e64 s[20:21], v173, v2
	v_cmp_gt_i32_e64 s[22:23], v174, v2
	v_cmp_gt_i32_e64 s[24:25], v175, v2
	v_cmp_gt_i32_e64 s[26:27], v176, v2
	v_cmp_gt_i32_e64 s[28:29], v177, v2
	v_cmp_gt_i32_e64 s[30:31], v178, v2
	v_cmp_gt_i32_e64 s[34:35], v179, v2
	v_cmp_gt_i32_e64 s[36:37], v180, v2
	v_cmp_gt_i32_e64 s[38:39], v181, v2
	v_cmp_gt_i32_e64 s[70:71], v6, v2
	s_min_u32 s2, s92, 8
	v_lshlrev_b32_e32 v2, 4, v4
	s_add_i32 s2, s92, s2
	v_and_b32_e32 v2, 0xc0, v2
	s_lshl_b32 s87, s2, 13
	v_lshl_or_b32 v2, v160, 8, v2
	v_readlane_b32 s2, v247, 4
	v_lshlrev_b32_e32 v5, 1, v4
	v_mov_b32_e32 v140, 0
	v_add_u32_e32 v185, s2, v2
	v_readlane_b32 s2, v247, 5
	s_movk_i32 s96, 0xc00
	s_add_i32 s91, s91, s92
	v_add_u32_e32 v187, s2, v2
	v_readlane_b32 s2, v247, 6
	s_add_i32 s93, s93, s3
	v_mov_b32_e32 v139, v131
	v_add_u32_e32 v188, s2, v2
	v_readlane_b32 s2, v247, 7
	s_mov_b32 s94, 2
	v_add_u32_e32 v183, s75, v134
	v_add_u32_e32 v189, s2, v2
	v_readlane_b32 s2, v247, 8
	v_add3_u32 v184, s76, v166, v134
	s_lshl_b32 s95, s92, 13
	v_add_u32_e32 v190, s2, v2
	v_readlane_b32 s2, v247, 9
	s_addk_i32 s87, 0x4000
	v_and_or_b32 v186, v5, 32, v3
	v_add_u32_e32 v191, s2, v2
	v_readlane_b32 s2, v247, 10
	s_add_i32 s86, s75, 0xc000
	s_mov_b32 s3, 0
	v_add_u32_e32 v192, s2, v2
	v_readlane_b32 s2, v247, 11
	v_mov_b32_e32 v202, 0
	v_mov_b32_e32 v3, v140
	v_add_u32_e32 v193, s2, v2
	v_readlane_b32 s2, v247, 12
	v_mov_b32_e32 v4, v140
	v_mov_b32_e32 v5, v140
	v_add_u32_e32 v194, s2, v2
	v_readlane_b32 s2, v247, 13
	v_mov_b32_e32 v6, v140
	v_mov_b32_e32 v7, v140
	v_add_u32_e32 v195, s2, v2
	v_readlane_b32 s2, v247, 14
	v_mov_b32_e32 v8, v140
	v_mov_b32_e32 v9, v140
	v_add_u32_e32 v196, s2, v2
	v_readlane_b32 s2, v247, 15
	v_mov_b32_e32 v10, v140
	v_mov_b32_e32 v11, v140
	v_add_u32_e32 v197, s2, v2
	v_readlane_b32 s2, v247, 16
	v_mov_b32_e32 v12, v140
	v_mov_b32_e32 v13, v140
	v_add_u32_e32 v198, s2, v2
	v_readlane_b32 s2, v247, 17
	v_mov_b32_e32 v14, v140
	v_mov_b32_e32 v15, v140
	v_add_u32_e32 v199, s2, v2
	v_readlane_b32 s2, v247, 21
	v_mov_b32_e32 v16, v140
	v_mov_b32_e32 v17, v140
	v_add_u32_e32 v200, s2, v2
	s_add_i32 s2, 0, 0x8000
	v_add_u32_e32 v201, s2, v2
	s_mov_b32 s2, 0
	v_mov_b32_e32 v2, 0
	v_mov_b32_e32 v18, 0
	v_mov_b32_e32 v19, v140
	v_mov_b32_e32 v20, v140
	v_mov_b32_e32 v21, v140
	v_mov_b32_e32 v22, v140
	v_mov_b32_e32 v23, v140
	v_add_u32_e32 v226, v201, v186
	s_nop 0
	s_nop 0
	s_nop 0
	s_nop 0
	s_nop 0
	s_nop 0
	s_nop 0
	v_mov_b32_e32 v24, v140
	v_mov_b32_e32 v25, v140
	v_mov_b32_e32 v26, v140
	v_mov_b32_e32 v27, v140
	v_mov_b32_e32 v28, v140
	v_mov_b32_e32 v29, v140
	v_mov_b32_e32 v30, v140
	v_mov_b32_e32 v31, v140
	v_mov_b32_e32 v32, v140
	v_mov_b32_e32 v33, v140
	v_mov_b64_e32 v[50:51], v[98:99]
	v_mov_b64_e32 v[52:53], v[100:101]
	v_mov_b64_e32 v[54:55], v[102:103]
	v_mov_b64_e32 v[56:57], v[104:105]
	v_mov_b64_e32 v[58:59], v[106:107]
	v_mov_b64_e32 v[60:61], v[108:109]
	v_mov_b64_e32 v[62:63], v[110:111]
	v_mov_b64_e32 v[64:65], v[112:113]
	s_branch .LBB0_2422

.Lcvdc_go:
	v_add_u32_e32 v89, s72, v84
	v_add_u32_e32 v90, 1040, v89
	ds_read2_b32 v[4:5], v89 offset0:0 offset1:32
	ds_read2_b32 v[6:7], v89 offset0:64 offset1:96
	ds_read2_b32 v[8:9], v89 offset0:128 offset1:160
	ds_read2_b32 v[10:11], v89 offset0:192 offset1:224
	ds_read2_b32 v[12:13], v90 offset0:0 offset1:32
	ds_read2_b32 v[14:15], v90 offset0:64 offset1:96
	ds_read2_b32 v[16:17], v90 offset0:128 offset1:160
	ds_read2_b32 v[18:19], v90 offset0:192 offset1:224
	ds_read2_b32 v[20:21], v89 offset0:16 offset1:48
	ds_read2_b32 v[22:23], v89 offset0:80 offset1:112
	ds_read2_b32 v[24:25], v89 offset0:144 offset1:176
	ds_read2_b32 v[26:27], v89 offset0:208 offset1:240
	ds_read2_b32 v[28:29], v90 offset0:16 offset1:48
	ds_read2_b32 v[30:31], v90 offset0:80 offset1:112
	ds_read2_b32 v[32:33], v90 offset0:144 offset1:176
	ds_read2_b32 v[34:35], v90 offset0:208 offset1:240
	s_cmp_eq_u32 s98, 0
	s_cselect_b64 vcc, -1, 0
	s_movk_i32 s7, 0x2000
	s_cselect_b32 s7, 0x8000, s7
	v_cndmask_b32_e32 v91, v87, v86, vcc
	s_waitcnt lgkmcnt(8)
	v_pk_mul_f32 v[4:5], v[4:5], v[100:101]
	v_pk_mul_f32 v[6:7], v[6:7], v[100:101]
	v_pk_mul_f32 v[8:9], v[8:9], v[100:101]
	v_pk_mul_f32 v[10:11], v[10:11], v[100:101]
	v_pk_mul_f32 v[12:13], v[12:13], v[100:101]
	v_pk_mul_f32 v[14:15], v[14:15], v[100:101]
	v_pk_mul_f32 v[16:17], v[16:17], v[100:101]
	v_pk_mul_f32 v[18:19], v[18:19], v[100:101]
	v_cvt_pk_fp8_f32 v92, v4, v5
	v_cvt_pk_fp8_f32 v93, v8, v9
	v_cvt_pk_fp8_f32 v94, v12, v13
	v_cvt_pk_fp8_f32 v95, v16, v17
	v_cvt_pk_fp8_f32 v92, v6, v7 op_sel:[0,0,1]
	v_cvt_pk_fp8_f32 v93, v10, v11 op_sel:[0,0,1]
	v_cvt_pk_fp8_f32 v94, v14, v15 op_sel:[0,0,1]
	v_cvt_pk_fp8_f32 v95, v18, v19 op_sel:[0,0,1]
	global_store_dwordx4 v91, v[92:95], s[84:85] nt
	s_waitcnt lgkmcnt(0)
	v_pk_mul_f32 v[20:21], v[20:21], v[100:101]
	v_pk_mul_f32 v[22:23], v[22:23], v[100:101]
	v_pk_mul_f32 v[24:25], v[24:25], v[100:101]
	v_pk_mul_f32 v[26:27], v[26:27], v[100:101]
	v_pk_mul_f32 v[28:29], v[28:29], v[100:101]
	v_pk_mul_f32 v[30:31], v[30:31], v[100:101]
	v_pk_mul_f32 v[32:33], v[32:33], v[100:101]
	v_pk_mul_f32 v[34:35], v[34:35], v[100:101]
	v_cvt_pk_fp8_f32 v96, v20, v21
	v_cvt_pk_fp8_f32 v97, v24, v25
	v_cvt_pk_fp8_f32 v98, v28, v29
	v_cvt_pk_fp8_f32 v99, v32, v33
	v_cvt_pk_fp8_f32 v96, v22, v23 op_sel:[0,0,1]
	v_cvt_pk_fp8_f32 v97, v26, v27 op_sel:[0,0,1]
	v_cvt_pk_fp8_f32 v98, v30, v31 op_sel:[0,0,1]
	v_cvt_pk_fp8_f32 v99, v34, v35 op_sel:[0,0,1]
	s_add_u32 s84, s84, s7
	s_addc_u32 s85, s85, 0
	global_store_dwordx4 v91, v[96:99], s[84:85] nt
	s_mov_b32 s32, 1
	s_cmp_eq_u32 s13, 0
	s_cbranch_scc1 .LBB0_2858
	s_mov_b32 s25, s12
	s_mov_b32 s7, s72
	s_mov_b32 s72, s86
	s_mov_b32 s86, s7
	s_branch .Lcvdc_loop
	s_nop 0
	s_nop 0
	s_nop 0
	s_nop 0
	s_nop 0
	s_nop 0
	s_nop 0
	s_nop 0
	s_nop 0
	s_nop 0
	s_nop 0
	s_nop 0
	s_nop 0
	s_nop 0
	s_nop 0
	s_nop 0
	s_nop 0
	s_nop 0
	s_nop 0
	s_nop 0
	s_nop 0
